# grid barriers 1-18: release hop removed, every workgroup polls the top arrival counter directly
# baseline (speedup 1.0000x reference)
; __device__ __forceinline__ unsigned xb_ld(unsigned* p)              { return __hip_atomic_load(p, __ATOMIC_RELAXED, __HIP_MEMORY_SCOPE_AGENT); }
; __device__ __forceinline__ unsigned xb_add(unsigned* p, unsigned v) { return __hip_atomic_fetch_add(p, v, __ATOMIC_RELAXED, __HIP_MEMORY_SCOPE_AGENT); }
; #define XB_SPIN(cond, bar) do { unsigned _sp = 0; while (cond) { __builtin_amdgcn_s_sleep(1); \
;     if ((++_sp & 255u) == 0u) { if (xb_ld(&(bar)[XB_TMO])) break; if (_sp > XB_SPIN_CAP) { atomicAdd(&(bar)[XB_TMO], 1u); break; } } } } while (0)
; #define SEAM(k) do { if (IN(k) && IN((k) + 1)) GRID_BAR(); } while (0)
; __device__ __forceinline__ void xcd_barrier(const XcdBarrier& b) {
;     asm volatile("s_waitcnt vmcnt(0)" ::: "memory");
;     __syncthreads();
;     if (threadIdx.x == 0) {
;         unsigned* bar = b.bar;
;         __builtin_amdgcn_s_waitcnt(0);
;         unsigned nloc = b.st[0], nx = b.st[1];
;         if (nloc == 0u) { xcd_barrier_complete(bar, b.x, nloc, nx); b.st[0] = nloc; b.st[1] = nx; }
;         const unsigned old = xb_add(&bar[XB_XSUB(b.x)], 1u);
;         const unsigned gen = old / nloc;
;         if (old + 1u == (gen + 1u) * nloc) {
;             __builtin_amdgcn_fence(__ATOMIC_RELEASE, "agent");
;             asm volatile("s_waitcnt vmcnt(0)" ::: "memory");
;             const unsigned og = xb_add(&bar[XB_TOP], 1u);
;             const unsigned tg = og / nx;
;             if (og + 1u == (tg + 1u) * nx) xb_add(&bar[XB_TOPGEN], 1u);
;             else XB_SPIN(xb_ld(&bar[XB_TOPGEN]) == tg, bar);
;             __builtin_amdgcn_fence(__ATOMIC_ACQUIRE, "agent");
;             xb_add(&bar[XB_XGEN(b.x)], 1u);
;             asm volatile("s_waitcnt vmcnt(0)" ::: "memory");
;         } else {
;             XB_SPIN(xb_ld(&bar[XB_XGEN(b.x)]) == gen, bar);
;             __builtin_amdgcn_fence(__ATOMIC_ACQUIRE, "agent");
;             asm volatile("s_waitcnt vmcnt(0)" ::: "memory");
;         }
;     }
;     __syncthreads();
; }
; __global__ void __launch_bounds__(NTHR, 2) fwd(Args args) {
;     ...
;     SEAM(1);
.LBB0_129:
	v_readlane_b32 s4, v255, 11
	v_readlane_b32 s5, v255, 12
	s_cmp_gt_i32 s5, 2
	s_cselect_b64 s[6:7], -1, 0
	s_and_b64 s[0:1], s[0:1], s[6:7]
	s_andn2_b64 vcc, exec, s[0:1]
	s_cbranch_vccnz .LBB0_183
	s_waitcnt vmcnt(0)
	s_waitcnt lgkmcnt(0)
	s_barrier
	s_mov_b64 s[0:1], exec
	v_readlane_b32 s4, v255, 7
	v_readlane_b32 s5, v255, 8
	s_and_b64 s[4:5], s[0:1], s[4:5]
	s_mov_b64 exec, s[4:5]
	s_cbranch_execz .LBB0_182
	s_add_i32 s3, 0, 0x20160
	v_mov_b32_e32 v1, s3
	ds_read_b64 v[2:3], v1
	v_readlane_b32 s8, v255, 6
	s_lshl_b32 s9, s8, 8
	s_add_u32 s10, s9, 0x5400
	v_mov_b32_e32 v4, s10
	v_mov_b32_e32 v5, 1
	s_waitcnt lgkmcnt(0)
	v_readfirstlane_b32 s12, v2
	v_readfirstlane_b32 s13, v3
	global_atomic_add v6, v4, v5, s[50:51] sc0
	s_add_u32 s14, s101, 1
	s_mul_i32 s15, s14, s12
	s_mul_i32 s16, s14, s13
	s_add_u32 s17, s9, 0x6400
	v_mov_b32_e32 v7, s17
	s_waitcnt vmcnt(0)
	v_readfirstlane_b32 s18, v6
	s_add_u32 s18, s18, 1
	s_cmp_lg_u32 s18, s15
	s_cbranch_scc1 .Lgb1_wait
	buffer_wbl2 sc1
	s_waitcnt vmcnt(0)
	v_mov_b32_e32 v8, 0x7400
	global_atomic_add v8, v5, s[50:51]
.Lgb1_wait:
	s_mov_b32 s20, 0
	v_mov_b32_e32 v7, 0x7400
.Lgb1_spin:
	global_load_dword v10, v7, s[50:51] sc1
	s_waitcnt vmcnt(0)
	v_readfirstlane_b32 s21, v10
	s_cmp_ge_u32 s21, s16
	s_cbranch_scc1 .Lgb1_acq
	s_sleep 1
	s_add_u32 s20, s20, 1
	s_cmp_lt_u32 s20, 0x100000
	s_cbranch_scc1 .Lgb1_spin

; __device__ __forceinline__ unsigned xb_ld(unsigned* p)              { return __hip_atomic_load(p, __ATOMIC_RELAXED, __HIP_MEMORY_SCOPE_AGENT); }
; __device__ __forceinline__ unsigned xb_add(unsigned* p, unsigned v) { return __hip_atomic_fetch_add(p, v, __ATOMIC_RELAXED, __HIP_MEMORY_SCOPE_AGENT); }
; #define XB_SPIN(cond, bar) do { unsigned _sp = 0; while (cond) { __builtin_amdgcn_s_sleep(1); \
;     if ((++_sp & 255u) == 0u) { if (xb_ld(&(bar)[XB_TMO])) break; if (_sp > XB_SPIN_CAP) { atomicAdd(&(bar)[XB_TMO], 1u); break; } } } } while (0)
; #define SEAM(k) do { if (IN(k) && IN((k) + 1)) GRID_BAR(); } while (0)
; __device__ __forceinline__ void xcd_barrier(const XcdBarrier& b) {
;     asm volatile("s_waitcnt vmcnt(0)" ::: "memory");
;     __syncthreads();
;     if (threadIdx.x == 0) {
;         unsigned* bar = b.bar;
;         __builtin_amdgcn_s_waitcnt(0);
;         unsigned nloc = b.st[0], nx = b.st[1];
;         if (nloc == 0u) { xcd_barrier_complete(bar, b.x, nloc, nx); b.st[0] = nloc; b.st[1] = nx; }
;         const unsigned old = xb_add(&bar[XB_XSUB(b.x)], 1u);
;         const unsigned gen = old / nloc;
;         if (old + 1u == (gen + 1u) * nloc) {
;             __builtin_amdgcn_fence(__ATOMIC_RELEASE, "agent");
;             asm volatile("s_waitcnt vmcnt(0)" ::: "memory");
;             const unsigned og = xb_add(&bar[XB_TOP], 1u);
;             const unsigned tg = og / nx;
;             if (og + 1u == (tg + 1u) * nx) xb_add(&bar[XB_TOPGEN], 1u);
;             else XB_SPIN(xb_ld(&bar[XB_TOPGEN]) == tg, bar);
;             __builtin_amdgcn_fence(__ATOMIC_ACQUIRE, "agent");
;             xb_add(&bar[XB_XGEN(b.x)], 1u);
;             asm volatile("s_waitcnt vmcnt(0)" ::: "memory");
;         } else {
;             XB_SPIN(xb_ld(&bar[XB_XGEN(b.x)]) == gen, bar);
;             __builtin_amdgcn_fence(__ATOMIC_ACQUIRE, "agent");
;             asm volatile("s_waitcnt vmcnt(0)" ::: "memory");
;         }
;     }
;     __syncthreads();
; }
; template <int L>
; __device__ __forceinline__ void layer(Frame& F, const XcdBarrier& bar, float* out, const int lo, const int hi) {
;     ...
;     SEAM(pb + 0);
.LBB0_224:
	v_readlane_b32 s0, v255, 11
	v_readlane_b32 s1, v255, 12
	s_cmp_gt_i32 s1, 3
	s_cselect_b64 s[6:7], -1, 0
	s_and_b64 s[0:1], s[10:11], s[6:7]
	s_andn2_b64 vcc, exec, s[0:1]
	s_cbranch_vccnz .LBB0_278
	s_waitcnt vmcnt(0)
	s_waitcnt lgkmcnt(0)
	s_barrier
	s_mov_b64 s[0:1], exec
	v_readlane_b32 s4, v255, 7
	v_readlane_b32 s5, v255, 8
	s_and_b64 s[4:5], s[0:1], s[4:5]
	s_mov_b64 exec, s[4:5]
	s_cbranch_execz .LBB0_277
	s_add_i32 s3, 0, 0x20160
	v_mov_b32_e32 v1, s3
	ds_read_b64 v[2:3], v1
	v_readlane_b32 s8, v255, 6
	s_lshl_b32 s9, s8, 8
	s_add_u32 s10, s9, 0x5400
	v_mov_b32_e32 v4, s10
	v_mov_b32_e32 v5, 1
	s_waitcnt lgkmcnt(0)
	v_readfirstlane_b32 s12, v2
	v_readfirstlane_b32 s13, v3
	global_atomic_add v6, v4, v5, s[50:51] sc0
	s_add_u32 s14, s101, 1
	s_mul_i32 s15, s14, s12
	s_mul_i32 s16, s14, s13
	s_add_u32 s17, s9, 0x6400
	v_mov_b32_e32 v7, s17
	s_waitcnt vmcnt(0)
	v_readfirstlane_b32 s18, v6
	s_add_u32 s18, s18, 1
	s_cmp_lg_u32 s18, s15
	s_cbranch_scc1 .Lgb2_wait
	buffer_wbl2 sc1
	s_waitcnt vmcnt(0)
	v_mov_b32_e32 v8, 0x7400
	global_atomic_add v8, v5, s[50:51]

; __device__ __forceinline__ unsigned xb_ld(unsigned* p)              { return __hip_atomic_load(p, __ATOMIC_RELAXED, __HIP_MEMORY_SCOPE_AGENT); }
; __device__ __forceinline__ unsigned xb_add(unsigned* p, unsigned v) { return __hip_atomic_fetch_add(p, v, __ATOMIC_RELAXED, __HIP_MEMORY_SCOPE_AGENT); }
; #define XB_SPIN(cond, bar) do { unsigned _sp = 0; while (cond) { __builtin_amdgcn_s_sleep(1); \
;     if ((++_sp & 255u) == 0u) { if (xb_ld(&(bar)[XB_TMO])) break; if (_sp > XB_SPIN_CAP) { atomicAdd(&(bar)[XB_TMO], 1u); break; } } } } while (0)
; #define SEAM(k) do { if (IN(k) && IN((k) + 1)) GRID_BAR(); } while (0)
; __device__ __forceinline__ void xcd_barrier(const XcdBarrier& b) {
;     asm volatile("s_waitcnt vmcnt(0)" ::: "memory");
;     __syncthreads();
;     if (threadIdx.x == 0) {
;         unsigned* bar = b.bar;
;         __builtin_amdgcn_s_waitcnt(0);
;         unsigned nloc = b.st[0], nx = b.st[1];
;         if (nloc == 0u) { xcd_barrier_complete(bar, b.x, nloc, nx); b.st[0] = nloc; b.st[1] = nx; }
;         const unsigned old = xb_add(&bar[XB_XSUB(b.x)], 1u);
;         const unsigned gen = old / nloc;
;         if (old + 1u == (gen + 1u) * nloc) {
;             __builtin_amdgcn_fence(__ATOMIC_RELEASE, "agent");
;             asm volatile("s_waitcnt vmcnt(0)" ::: "memory");
;             const unsigned og = xb_add(&bar[XB_TOP], 1u);
;             const unsigned tg = og / nx;
;             if (og + 1u == (tg + 1u) * nx) xb_add(&bar[XB_TOPGEN], 1u);
;             else XB_SPIN(xb_ld(&bar[XB_TOPGEN]) == tg, bar);
;             __builtin_amdgcn_fence(__ATOMIC_ACQUIRE, "agent");
;             xb_add(&bar[XB_XGEN(b.x)], 1u);
;             asm volatile("s_waitcnt vmcnt(0)" ::: "memory");
;         } else {
;             XB_SPIN(xb_ld(&bar[XB_XGEN(b.x)]) == gen, bar);
;             __builtin_amdgcn_fence(__ATOMIC_ACQUIRE, "agent");
;             asm volatile("s_waitcnt vmcnt(0)" ::: "memory");
;         }
;     }
;     __syncthreads();
; }
; template <int L>
; __device__ __forceinline__ void layer(Frame& F, const XcdBarrier& bar, float* out, const int lo, const int hi) {
;     ...
;     SEAM(pb + 1);
.LBB0_303:
	v_readlane_b32 s4, v255, 11
	v_readlane_b32 s5, v255, 12
	s_cmp_gt_i32 s5, 4
	s_cselect_b64 s[6:7], -1, 0
	s_and_b64 s[0:1], s[0:1], s[6:7]
	s_andn2_b64 vcc, exec, s[0:1]
	s_cbranch_vccnz .LBB0_357
	s_waitcnt vmcnt(0)
	s_waitcnt lgkmcnt(0)
	s_barrier
	s_mov_b64 s[0:1], exec
	v_readlane_b32 s4, v255, 7
	v_readlane_b32 s5, v255, 8
	s_and_b64 s[4:5], s[0:1], s[4:5]
	s_mov_b64 exec, s[4:5]
	s_cbranch_execz .LBB0_356
	s_add_i32 s3, 0, 0x20160
	v_mov_b32_e32 v1, s3
	ds_read_b64 v[2:3], v1
	v_readlane_b32 s8, v255, 6
	s_lshl_b32 s9, s8, 8
	s_add_u32 s10, s9, 0x5400
	v_mov_b32_e32 v4, s10
	v_mov_b32_e32 v5, 1
	s_waitcnt lgkmcnt(0)
	v_readfirstlane_b32 s12, v2
	v_readfirstlane_b32 s13, v3
	global_atomic_add v6, v4, v5, s[50:51] sc0
	s_add_u32 s14, s101, 1
	s_mul_i32 s15, s14, s12
	s_mul_i32 s16, s14, s13
	s_add_u32 s17, s9, 0x6400
	v_mov_b32_e32 v7, s17
	s_waitcnt vmcnt(0)
	v_readfirstlane_b32 s18, v6
	s_add_u32 s18, s18, 1
	s_cmp_lg_u32 s18, s15
	s_cbranch_scc1 .Lgb3_wait
	buffer_wbl2 sc1
	s_waitcnt vmcnt(0)
	v_mov_b32_e32 v8, 0x7400
	global_atomic_add v8, v5, s[50:51]

; __device__ __forceinline__ unsigned xb_ld(unsigned* p)              { return __hip_atomic_load(p, __ATOMIC_RELAXED, __HIP_MEMORY_SCOPE_AGENT); }
; __device__ __forceinline__ unsigned xb_add(unsigned* p, unsigned v) { return __hip_atomic_fetch_add(p, v, __ATOMIC_RELAXED, __HIP_MEMORY_SCOPE_AGENT); }
; #define XB_SPIN(cond, bar) do { unsigned _sp = 0; while (cond) { __builtin_amdgcn_s_sleep(1); \
;     if ((++_sp & 255u) == 0u) { if (xb_ld(&(bar)[XB_TMO])) break; if (_sp > XB_SPIN_CAP) { atomicAdd(&(bar)[XB_TMO], 1u); break; } } } } while (0)
; #define GRID_BAR() do { if (N_LAUNCHES == 1) xcd_barrier(bar); } while (0)
; __device__ __forceinline__ void xcd_barrier(const XcdBarrier& b) {
;     asm volatile("s_waitcnt vmcnt(0)" ::: "memory");
;     __syncthreads();
;     if (threadIdx.x == 0) {
;         unsigned* bar = b.bar;
;         __builtin_amdgcn_s_waitcnt(0);
;         unsigned nloc = b.st[0], nx = b.st[1];
;         if (nloc == 0u) { xcd_barrier_complete(bar, b.x, nloc, nx); b.st[0] = nloc; b.st[1] = nx; }
;         const unsigned old = xb_add(&bar[XB_XSUB(b.x)], 1u);
;         const unsigned gen = old / nloc;
;         if (old + 1u == (gen + 1u) * nloc) {
;             __builtin_amdgcn_fence(__ATOMIC_RELEASE, "agent");
;             asm volatile("s_waitcnt vmcnt(0)" ::: "memory");
;             const unsigned og = xb_add(&bar[XB_TOP], 1u);
;             const unsigned tg = og / nx;
;             if (og + 1u == (tg + 1u) * nx) xb_add(&bar[XB_TOPGEN], 1u);
;             else XB_SPIN(xb_ld(&bar[XB_TOPGEN]) == tg, bar);
;             __builtin_amdgcn_fence(__ATOMIC_ACQUIRE, "agent");
;             xb_add(&bar[XB_XGEN(b.x)], 1u);
;             asm volatile("s_waitcnt vmcnt(0)" ::: "memory");
;         } else {
;             XB_SPIN(xb_ld(&bar[XB_XGEN(b.x)]) == gen, bar);
;             __builtin_amdgcn_fence(__ATOMIC_ACQUIRE, "agent");
;             asm volatile("s_waitcnt vmcnt(0)" ::: "memory");
;         }
;     }
;     __syncthreads();
; }
; template <int L>
; __device__ __forceinline__ void layer(Frame& F, const XcdBarrier& bar, float* out, const int lo, const int hi) {
;     ...
;         GRID_BAR();
.LBB0_451:
	s_waitcnt vmcnt(0)
	s_waitcnt lgkmcnt(0)
	s_barrier
	s_mov_b64 s[0:1], exec
	v_readlane_b32 s6, v255, 7
	v_readlane_b32 s7, v255, 8
	s_and_b64 s[6:7], s[0:1], s[6:7]
	s_mov_b64 exec, s[6:7]
	s_cbranch_execz .LBB0_503
	s_add_i32 s3, 0, 0x20160
	v_mov_b32_e32 v1, s3
	ds_read_b64 v[2:3], v1
	v_readlane_b32 s8, v255, 6
	s_lshl_b32 s9, s8, 8
	s_add_u32 s10, s9, 0x5400
	v_mov_b32_e32 v4, s10
	v_mov_b32_e32 v5, 1
	s_waitcnt lgkmcnt(0)
	v_readfirstlane_b32 s12, v2
	v_readfirstlane_b32 s13, v3
	global_atomic_add v6, v4, v5, s[50:51] sc0
	s_add_u32 s14, s101, 1
	s_mul_i32 s15, s14, s12
	s_mul_i32 s16, s14, s13
	s_add_u32 s17, s9, 0x6400
	v_mov_b32_e32 v7, s17
	s_waitcnt vmcnt(0)
	v_readfirstlane_b32 s18, v6
	s_add_u32 s18, s18, 1
	s_cmp_lg_u32 s18, s15
	s_cbranch_scc1 .Lgb4_wait
	buffer_wbl2 sc1
	s_waitcnt vmcnt(0)
	v_mov_b32_e32 v8, 0x7400
	global_atomic_add v8, v5, s[50:51]

; __device__ __forceinline__ unsigned xb_ld(unsigned* p)              { return __hip_atomic_load(p, __ATOMIC_RELAXED, __HIP_MEMORY_SCOPE_AGENT); }
; __device__ __forceinline__ unsigned xb_add(unsigned* p, unsigned v) { return __hip_atomic_fetch_add(p, v, __ATOMIC_RELAXED, __HIP_MEMORY_SCOPE_AGENT); }
; #define XB_SPIN(cond, bar) do { unsigned _sp = 0; while (cond) { __builtin_amdgcn_s_sleep(1); \
;     if ((++_sp & 255u) == 0u) { if (xb_ld(&(bar)[XB_TMO])) break; if (_sp > XB_SPIN_CAP) { atomicAdd(&(bar)[XB_TMO], 1u); break; } } } } while (0)
; #define SEAM(k) do { if (IN(k) && IN((k) + 1)) GRID_BAR(); } while (0)
; __device__ __forceinline__ void xcd_barrier(const XcdBarrier& b) {
;     asm volatile("s_waitcnt vmcnt(0)" ::: "memory");
;     __syncthreads();
;     if (threadIdx.x == 0) {
;         unsigned* bar = b.bar;
;         __builtin_amdgcn_s_waitcnt(0);
;         unsigned nloc = b.st[0], nx = b.st[1];
;         if (nloc == 0u) { xcd_barrier_complete(bar, b.x, nloc, nx); b.st[0] = nloc; b.st[1] = nx; }
;         const unsigned old = xb_add(&bar[XB_XSUB(b.x)], 1u);
;         const unsigned gen = old / nloc;
;         if (old + 1u == (gen + 1u) * nloc) {
;             __builtin_amdgcn_fence(__ATOMIC_RELEASE, "agent");
;             asm volatile("s_waitcnt vmcnt(0)" ::: "memory");
;             const unsigned og = xb_add(&bar[XB_TOP], 1u);
;             const unsigned tg = og / nx;
;             if (og + 1u == (tg + 1u) * nx) xb_add(&bar[XB_TOPGEN], 1u);
;             else XB_SPIN(xb_ld(&bar[XB_TOPGEN]) == tg, bar);
;             __builtin_amdgcn_fence(__ATOMIC_ACQUIRE, "agent");
;             xb_add(&bar[XB_XGEN(b.x)], 1u);
;             asm volatile("s_waitcnt vmcnt(0)" ::: "memory");
;         } else {
;             XB_SPIN(xb_ld(&bar[XB_XGEN(b.x)]) == gen, bar);
;             __builtin_amdgcn_fence(__ATOMIC_ACQUIRE, "agent");
;             asm volatile("s_waitcnt vmcnt(0)" ::: "memory");
;         }
;     }
;     __syncthreads();
; }
; template <int L>
; __device__ __forceinline__ void layer(Frame& F, const XcdBarrier& bar, float* out, const int lo, const int hi) {
;     ...
;     SEAM(pb + 2);
.LBB0_946:
	v_readlane_b32 s0, v255, 11
	v_readlane_b32 s1, v255, 12
	s_cmp_gt_i32 s1, 5
	v_readlane_b32 s0, v255, 30
	s_cselect_b64 s[6:7], -1, 0
	v_readlane_b32 s1, v255, 31
	s_and_b64 s[0:1], s[0:1], s[6:7]
	s_andn2_b64 vcc, exec, s[0:1]
	s_cbranch_vccnz .LBB0_1000
	s_waitcnt vmcnt(0)
	s_waitcnt lgkmcnt(0)
	s_barrier
	s_mov_b64 s[0:1], exec
	v_readlane_b32 s8, v255, 7
	v_readlane_b32 s9, v255, 8
	s_and_b64 s[8:9], s[0:1], s[8:9]
	s_mov_b64 exec, s[8:9]
	s_cbranch_execz .LBB0_999
	s_add_i32 s3, 0, 0x20160
	v_mov_b32_e32 v1, s3
	ds_read_b64 v[2:3], v1
	v_readlane_b32 s8, v255, 6
	s_lshl_b32 s9, s8, 8
	s_add_u32 s10, s9, 0x5400
	v_mov_b32_e32 v4, s10
	v_mov_b32_e32 v5, 1
	s_waitcnt lgkmcnt(0)
	v_readfirstlane_b32 s12, v2
	v_readfirstlane_b32 s13, v3
	global_atomic_add v6, v4, v5, s[50:51] sc0
	s_add_u32 s14, s101, 1
	s_mul_i32 s15, s14, s12
	s_mul_i32 s16, s14, s13
	s_add_u32 s17, s9, 0x6400
	v_mov_b32_e32 v7, s17
	s_waitcnt vmcnt(0)
	v_readfirstlane_b32 s18, v6
	s_add_u32 s18, s18, 1
	s_cmp_lg_u32 s18, s15
	s_cbranch_scc1 .Lgb5_wait
	buffer_wbl2 sc1
	s_waitcnt vmcnt(0)
	v_mov_b32_e32 v8, 0x7400
	global_atomic_add v8, v5, s[50:51]

; __device__ __forceinline__ unsigned xb_ld(unsigned* p)              { return __hip_atomic_load(p, __ATOMIC_RELAXED, __HIP_MEMORY_SCOPE_AGENT); }
; __device__ __forceinline__ unsigned xb_add(unsigned* p, unsigned v) { return __hip_atomic_fetch_add(p, v, __ATOMIC_RELAXED, __HIP_MEMORY_SCOPE_AGENT); }
; #define XB_SPIN(cond, bar) do { unsigned _sp = 0; while (cond) { __builtin_amdgcn_s_sleep(1); \
;     if ((++_sp & 255u) == 0u) { if (xb_ld(&(bar)[XB_TMO])) break; if (_sp > XB_SPIN_CAP) { atomicAdd(&(bar)[XB_TMO], 1u); break; } } } } while (0)
; #define SEAM(k) do { if (IN(k) && IN((k) + 1)) GRID_BAR(); } while (0)
; __device__ __forceinline__ void xcd_barrier(const XcdBarrier& b) {
;     asm volatile("s_waitcnt vmcnt(0)" ::: "memory");
;     __syncthreads();
;     if (threadIdx.x == 0) {
;         unsigned* bar = b.bar;
;         __builtin_amdgcn_s_waitcnt(0);
;         unsigned nloc = b.st[0], nx = b.st[1];
;         if (nloc == 0u) { xcd_barrier_complete(bar, b.x, nloc, nx); b.st[0] = nloc; b.st[1] = nx; }
;         const unsigned old = xb_add(&bar[XB_XSUB(b.x)], 1u);
;         const unsigned gen = old / nloc;
;         if (old + 1u == (gen + 1u) * nloc) {
;             __builtin_amdgcn_fence(__ATOMIC_RELEASE, "agent");
;             asm volatile("s_waitcnt vmcnt(0)" ::: "memory");
;             const unsigned og = xb_add(&bar[XB_TOP], 1u);
;             const unsigned tg = og / nx;
;             if (og + 1u == (tg + 1u) * nx) xb_add(&bar[XB_TOPGEN], 1u);
;             else XB_SPIN(xb_ld(&bar[XB_TOPGEN]) == tg, bar);
;             __builtin_amdgcn_fence(__ATOMIC_ACQUIRE, "agent");
;             xb_add(&bar[XB_XGEN(b.x)], 1u);
;             asm volatile("s_waitcnt vmcnt(0)" ::: "memory");
;         } else {
;             XB_SPIN(xb_ld(&bar[XB_XGEN(b.x)]) == gen, bar);
;             __builtin_amdgcn_fence(__ATOMIC_ACQUIRE, "agent");
;             asm volatile("s_waitcnt vmcnt(0)" ::: "memory");
;         }
;     }
;     __syncthreads();
; }
; template <int L>
; __device__ __forceinline__ void layer(Frame& F, const XcdBarrier& bar, float* out, const int lo, const int hi) {
;     ...
;     SEAM(pb + 3);
.LBB0_1025:
	v_readlane_b32 s6, v255, 11
	v_readlane_b32 s7, v255, 12
	s_cmp_gt_i32 s7, 6
	s_cselect_b64 s[6:7], -1, 0
	s_and_b64 s[0:1], s[0:1], s[6:7]
	s_andn2_b64 vcc, exec, s[0:1]
	s_cbranch_vccnz .LBB0_1079
	s_waitcnt vmcnt(0)
	s_waitcnt vmcnt(0) lgkmcnt(0)
	s_barrier
	s_mov_b64 s[0:1], exec
	v_readlane_b32 s8, v255, 7
	v_readlane_b32 s9, v255, 8
	s_and_b64 s[8:9], s[0:1], s[8:9]
	s_mov_b64 exec, s[8:9]
	s_cbranch_execz .LBB0_1078
	s_add_i32 s3, 0, 0x20160
	v_mov_b32_e32 v1, s3
	ds_read_b64 v[2:3], v1
	v_readlane_b32 s8, v255, 6
	s_lshl_b32 s9, s8, 8
	s_add_u32 s10, s9, 0x5400
	v_mov_b32_e32 v4, s10
	v_mov_b32_e32 v5, 1
	s_waitcnt lgkmcnt(0)
	v_readfirstlane_b32 s12, v2
	v_readfirstlane_b32 s13, v3
	global_atomic_add v6, v4, v5, s[50:51] sc0
	s_add_u32 s14, s101, 1
	s_mul_i32 s15, s14, s12
	s_mul_i32 s16, s14, s13
	s_add_u32 s17, s9, 0x6400
	v_mov_b32_e32 v7, s17
	s_waitcnt vmcnt(0)
	v_readfirstlane_b32 s18, v6
	s_add_u32 s18, s18, 1
	s_cmp_lg_u32 s18, s15
	s_cbranch_scc1 .Lgb6_wait
	buffer_wbl2 sc1
	s_waitcnt vmcnt(0)
	v_mov_b32_e32 v8, 0x7400
	global_atomic_add v8, v5, s[50:51]

; __device__ __forceinline__ unsigned xb_ld(unsigned* p)              { return __hip_atomic_load(p, __ATOMIC_RELAXED, __HIP_MEMORY_SCOPE_AGENT); }
; __device__ __forceinline__ unsigned xb_add(unsigned* p, unsigned v) { return __hip_atomic_fetch_add(p, v, __ATOMIC_RELAXED, __HIP_MEMORY_SCOPE_AGENT); }
; #define XB_SPIN(cond, bar) do { unsigned _sp = 0; while (cond) { __builtin_amdgcn_s_sleep(1); \
;     if ((++_sp & 255u) == 0u) { if (xb_ld(&(bar)[XB_TMO])) break; if (_sp > XB_SPIN_CAP) { atomicAdd(&(bar)[XB_TMO], 1u); break; } } } } while (0)
; #define SEAM(k) do { if (IN(k) && IN((k) + 1)) GRID_BAR(); } while (0)
; __device__ __forceinline__ void xcd_barrier(const XcdBarrier& b) {
;     asm volatile("s_waitcnt vmcnt(0)" ::: "memory");
;     __syncthreads();
;     if (threadIdx.x == 0) {
;         unsigned* bar = b.bar;
;         __builtin_amdgcn_s_waitcnt(0);
;         unsigned nloc = b.st[0], nx = b.st[1];
;         if (nloc == 0u) { xcd_barrier_complete(bar, b.x, nloc, nx); b.st[0] = nloc; b.st[1] = nx; }
;         const unsigned old = xb_add(&bar[XB_XSUB(b.x)], 1u);
;         const unsigned gen = old / nloc;
;         if (old + 1u == (gen + 1u) * nloc) {
;             __builtin_amdgcn_fence(__ATOMIC_RELEASE, "agent");
;             asm volatile("s_waitcnt vmcnt(0)" ::: "memory");
;             const unsigned og = xb_add(&bar[XB_TOP], 1u);
;             const unsigned tg = og / nx;
;             if (og + 1u == (tg + 1u) * nx) xb_add(&bar[XB_TOPGEN], 1u);
;             else XB_SPIN(xb_ld(&bar[XB_TOPGEN]) == tg, bar);
;             __builtin_amdgcn_fence(__ATOMIC_ACQUIRE, "agent");
;             xb_add(&bar[XB_XGEN(b.x)], 1u);
;             asm volatile("s_waitcnt vmcnt(0)" ::: "memory");
;         } else {
;             XB_SPIN(xb_ld(&bar[XB_XGEN(b.x)]) == gen, bar);
;             __builtin_amdgcn_fence(__ATOMIC_ACQUIRE, "agent");
;             asm volatile("s_waitcnt vmcnt(0)" ::: "memory");
;         }
;     }
;     __syncthreads();
; }
; template <int L>
; __device__ __forceinline__ void layer(Frame& F, const XcdBarrier& bar, float* out, const int lo, const int hi) {
;     ...
;     SEAM(pb + 4);
.LBB0_1090:
	v_readlane_b32 s6, v255, 11
	v_readlane_b32 s7, v255, 12
	s_cmp_gt_i32 s7, 7
	s_cselect_b64 s[6:7], -1, 0
	s_and_b64 s[0:1], s[0:1], s[6:7]
	s_andn2_b64 vcc, exec, s[0:1]
	s_cbranch_vccnz .LBB0_1144
	s_waitcnt vmcnt(0)
	s_waitcnt vmcnt(0) lgkmcnt(0)
	s_barrier
	s_mov_b64 s[0:1], exec
	v_readlane_b32 s8, v255, 7
	v_readlane_b32 s9, v255, 8
	s_and_b64 s[8:9], s[0:1], s[8:9]
	s_mov_b64 exec, s[8:9]
	s_cbranch_execz .LBB0_1143
	s_add_i32 s3, 0, 0x20160
	v_mov_b32_e32 v1, s3
	ds_read_b64 v[2:3], v1
	v_readlane_b32 s8, v255, 6
	s_lshl_b32 s9, s8, 8
	s_add_u32 s10, s9, 0x5400
	v_mov_b32_e32 v4, s10
	v_mov_b32_e32 v5, 1
	s_waitcnt lgkmcnt(0)
	v_readfirstlane_b32 s12, v2
	v_readfirstlane_b32 s13, v3
	global_atomic_add v6, v4, v5, s[50:51] sc0
	s_add_u32 s14, s101, 1
	s_mul_i32 s15, s14, s12
	s_mul_i32 s16, s14, s13
	s_add_u32 s17, s9, 0x6400
	v_mov_b32_e32 v7, s17
	s_waitcnt vmcnt(0)
	v_readfirstlane_b32 s18, v6
	s_add_u32 s18, s18, 1
	s_cmp_lg_u32 s18, s15
	s_cbranch_scc1 .Lgb7_wait
	buffer_wbl2 sc1
	s_waitcnt vmcnt(0)
	v_mov_b32_e32 v8, 0x7400
	global_atomic_add v8, v5, s[50:51]

; __device__ __forceinline__ unsigned xb_ld(unsigned* p)              { return __hip_atomic_load(p, __ATOMIC_RELAXED, __HIP_MEMORY_SCOPE_AGENT); }
; __device__ __forceinline__ unsigned xb_add(unsigned* p, unsigned v) { return __hip_atomic_fetch_add(p, v, __ATOMIC_RELAXED, __HIP_MEMORY_SCOPE_AGENT); }
; #define XB_SPIN(cond, bar) do { unsigned _sp = 0; while (cond) { __builtin_amdgcn_s_sleep(1); \
;     if ((++_sp & 255u) == 0u) { if (xb_ld(&(bar)[XB_TMO])) break; if (_sp > XB_SPIN_CAP) { atomicAdd(&(bar)[XB_TMO], 1u); break; } } } } while (0)
; #define SEAM(k) do { if (IN(k) && IN((k) + 1)) GRID_BAR(); } while (0)
; __device__ __forceinline__ void xcd_barrier(const XcdBarrier& b) {
;     asm volatile("s_waitcnt vmcnt(0)" ::: "memory");
;     __syncthreads();
;     if (threadIdx.x == 0) {
;         unsigned* bar = b.bar;
;         __builtin_amdgcn_s_waitcnt(0);
;         unsigned nloc = b.st[0], nx = b.st[1];
;         if (nloc == 0u) { xcd_barrier_complete(bar, b.x, nloc, nx); b.st[0] = nloc; b.st[1] = nx; }
;         const unsigned old = xb_add(&bar[XB_XSUB(b.x)], 1u);
;         const unsigned gen = old / nloc;
;         if (old + 1u == (gen + 1u) * nloc) {
;             __builtin_amdgcn_fence(__ATOMIC_RELEASE, "agent");
;             asm volatile("s_waitcnt vmcnt(0)" ::: "memory");
;             const unsigned og = xb_add(&bar[XB_TOP], 1u);
;             const unsigned tg = og / nx;
;             if (og + 1u == (tg + 1u) * nx) xb_add(&bar[XB_TOPGEN], 1u);
;             else XB_SPIN(xb_ld(&bar[XB_TOPGEN]) == tg, bar);
;             __builtin_amdgcn_fence(__ATOMIC_ACQUIRE, "agent");
;             xb_add(&bar[XB_XGEN(b.x)], 1u);
;             asm volatile("s_waitcnt vmcnt(0)" ::: "memory");
;         } else {
;             XB_SPIN(xb_ld(&bar[XB_XGEN(b.x)]) == gen, bar);
;             __builtin_amdgcn_fence(__ATOMIC_ACQUIRE, "agent");
;             asm volatile("s_waitcnt vmcnt(0)" ::: "memory");
;         }
;     }
;     __syncthreads();
; }
; template <int L>
; __device__ __forceinline__ void layer(Frame& F, const XcdBarrier& bar, float* out, const int lo, const int hi) {
;     ...
;         SEAM(pb + 5);
.LBB0_1161:
	v_readlane_b32 s6, v255, 11
	v_readlane_b32 s7, v255, 12
	s_cmp_gt_i32 s7, 8
	s_cselect_b64 s[6:7], -1, 0
	s_and_b64 s[0:1], s[0:1], s[6:7]
	s_andn2_b64 vcc, exec, s[0:1]
	s_cbranch_vccnz .LBB0_1215
	s_waitcnt vmcnt(0)
	s_waitcnt vmcnt(0) lgkmcnt(0)
	s_barrier
	s_mov_b64 s[0:1], exec
	v_readlane_b32 s8, v255, 7
	v_readlane_b32 s9, v255, 8
	s_and_b64 s[8:9], s[0:1], s[8:9]
	s_mov_b64 exec, s[8:9]
	s_cbranch_execz .LBB0_1214
	s_add_i32 s3, 0, 0x20160
	v_mov_b32_e32 v1, s3
	ds_read_b64 v[2:3], v1
	v_readlane_b32 s8, v255, 6
	s_lshl_b32 s9, s8, 8
	s_add_u32 s10, s9, 0x5400
	v_mov_b32_e32 v4, s10
	v_mov_b32_e32 v5, 1
	s_waitcnt lgkmcnt(0)
	v_readfirstlane_b32 s12, v2
	v_readfirstlane_b32 s13, v3
	global_atomic_add v6, v4, v5, s[50:51] sc0
	s_add_u32 s14, s101, 1
	s_mul_i32 s15, s14, s12
	s_mul_i32 s16, s14, s13
	s_add_u32 s17, s9, 0x6400
	v_mov_b32_e32 v7, s17
	s_waitcnt vmcnt(0)
	v_readfirstlane_b32 s18, v6
	s_add_u32 s18, s18, 1
	s_cmp_lg_u32 s18, s15
	s_cbranch_scc1 .Lgb8_wait
	buffer_wbl2 sc1
	s_waitcnt vmcnt(0)
	v_mov_b32_e32 v8, 0x7400
	global_atomic_add v8, v5, s[50:51]

; __device__ __forceinline__ unsigned xb_ld(unsigned* p)              { return __hip_atomic_load(p, __ATOMIC_RELAXED, __HIP_MEMORY_SCOPE_AGENT); }
; __device__ __forceinline__ unsigned xb_add(unsigned* p, unsigned v) { return __hip_atomic_fetch_add(p, v, __ATOMIC_RELAXED, __HIP_MEMORY_SCOPE_AGENT); }
; #define XB_SPIN(cond, bar) do { unsigned _sp = 0; while (cond) { __builtin_amdgcn_s_sleep(1); \
;     if ((++_sp & 255u) == 0u) { if (xb_ld(&(bar)[XB_TMO])) break; if (_sp > XB_SPIN_CAP) { atomicAdd(&(bar)[XB_TMO], 1u); break; } } } } while (0)
; #define SEAM(k) do { if (IN(k) && IN((k) + 1)) GRID_BAR(); } while (0)
; __device__ __forceinline__ void xcd_barrier(const XcdBarrier& b) {
;     asm volatile("s_waitcnt vmcnt(0)" ::: "memory");
;     __syncthreads();
;     if (threadIdx.x == 0) {
;         unsigned* bar = b.bar;
;         __builtin_amdgcn_s_waitcnt(0);
;         unsigned nloc = b.st[0], nx = b.st[1];
;         if (nloc == 0u) { xcd_barrier_complete(bar, b.x, nloc, nx); b.st[0] = nloc; b.st[1] = nx; }
;         const unsigned old = xb_add(&bar[XB_XSUB(b.x)], 1u);
;         const unsigned gen = old / nloc;
;         if (old + 1u == (gen + 1u) * nloc) {
;             __builtin_amdgcn_fence(__ATOMIC_RELEASE, "agent");
;             asm volatile("s_waitcnt vmcnt(0)" ::: "memory");
;             const unsigned og = xb_add(&bar[XB_TOP], 1u);
;             const unsigned tg = og / nx;
;             if (og + 1u == (tg + 1u) * nx) xb_add(&bar[XB_TOPGEN], 1u);
;             else XB_SPIN(xb_ld(&bar[XB_TOPGEN]) == tg, bar);
;             __builtin_amdgcn_fence(__ATOMIC_ACQUIRE, "agent");
;             xb_add(&bar[XB_XGEN(b.x)], 1u);
;             asm volatile("s_waitcnt vmcnt(0)" ::: "memory");
;         } else {
;             XB_SPIN(xb_ld(&bar[XB_XGEN(b.x)]) == gen, bar);
;             __builtin_amdgcn_fence(__ATOMIC_ACQUIRE, "agent");
;             asm volatile("s_waitcnt vmcnt(0)" ::: "memory");
;         }
;     }
;     __syncthreads();
; }
; template <int L>
; __device__ __forceinline__ void layer(Frame& F, const XcdBarrier& bar, float* out, const int lo, const int hi) {
;     ...
;         SEAM(pb + 6);
.LBB0_1244:
	v_readlane_b32 s6, v255, 11
	v_readlane_b32 s7, v255, 12
	s_cmp_gt_i32 s7, 9
	s_cselect_b64 s[6:7], -1, 0
	s_and_b64 s[0:1], s[0:1], s[6:7]
	s_andn2_b64 vcc, exec, s[0:1]
	s_cbranch_vccnz .LBB0_1298
	s_waitcnt vmcnt(0)
	s_waitcnt vmcnt(0) lgkmcnt(0)
	s_barrier
	s_mov_b64 s[0:1], exec
	v_readlane_b32 s8, v255, 7
	v_readlane_b32 s9, v255, 8
	s_and_b64 s[8:9], s[0:1], s[8:9]
	s_mov_b64 exec, s[8:9]
	s_cbranch_execz .LBB0_1297
	s_add_i32 s3, 0, 0x20160
	v_mov_b32_e32 v1, s3
	ds_read_b64 v[2:3], v1
	v_readlane_b32 s8, v255, 6
	s_lshl_b32 s9, s8, 8
	s_add_u32 s10, s9, 0x5400
	v_mov_b32_e32 v4, s10
	v_mov_b32_e32 v5, 1
	s_waitcnt lgkmcnt(0)
	v_readfirstlane_b32 s12, v2
	v_readfirstlane_b32 s13, v3
	global_atomic_add v6, v4, v5, s[50:51] sc0
	s_add_u32 s14, s101, 1
	s_mul_i32 s15, s14, s12
	s_mul_i32 s16, s14, s13
	s_add_u32 s17, s9, 0x6400
	v_mov_b32_e32 v7, s17
	s_waitcnt vmcnt(0)
	v_readfirstlane_b32 s18, v6
	s_add_u32 s18, s18, 1
	s_cmp_lg_u32 s18, s15
	s_cbranch_scc1 .Lgb9_wait
	buffer_wbl2 sc1
	s_waitcnt vmcnt(0)
	v_mov_b32_e32 v8, 0x7400
	global_atomic_add v8, v5, s[50:51]

; __device__ __forceinline__ unsigned xb_ld(unsigned* p)              { return __hip_atomic_load(p, __ATOMIC_RELAXED, __HIP_MEMORY_SCOPE_AGENT); }
; __device__ __forceinline__ unsigned xb_add(unsigned* p, unsigned v) { return __hip_atomic_fetch_add(p, v, __ATOMIC_RELAXED, __HIP_MEMORY_SCOPE_AGENT); }
; #define XB_SPIN(cond, bar) do { unsigned _sp = 0; while (cond) { __builtin_amdgcn_s_sleep(1); \
;     if ((++_sp & 255u) == 0u) { if (xb_ld(&(bar)[XB_TMO])) break; if (_sp > XB_SPIN_CAP) { atomicAdd(&(bar)[XB_TMO], 1u); break; } } } } while (0)
; #define SEAM(k) do { if (IN(k) && IN((k) + 1)) GRID_BAR(); } while (0)
; __device__ __forceinline__ void xcd_barrier(const XcdBarrier& b) {
;     asm volatile("s_waitcnt vmcnt(0)" ::: "memory");
;     __syncthreads();
;     if (threadIdx.x == 0) {
;         unsigned* bar = b.bar;
;         __builtin_amdgcn_s_waitcnt(0);
;         unsigned nloc = b.st[0], nx = b.st[1];
;         if (nloc == 0u) { xcd_barrier_complete(bar, b.x, nloc, nx); b.st[0] = nloc; b.st[1] = nx; }
;         const unsigned old = xb_add(&bar[XB_XSUB(b.x)], 1u);
;         const unsigned gen = old / nloc;
;         if (old + 1u == (gen + 1u) * nloc) {
;             __builtin_amdgcn_fence(__ATOMIC_RELEASE, "agent");
;             asm volatile("s_waitcnt vmcnt(0)" ::: "memory");
;             const unsigned og = xb_add(&bar[XB_TOP], 1u);
;             const unsigned tg = og / nx;
;             if (og + 1u == (tg + 1u) * nx) xb_add(&bar[XB_TOPGEN], 1u);
;             else XB_SPIN(xb_ld(&bar[XB_TOPGEN]) == tg, bar);
;             __builtin_amdgcn_fence(__ATOMIC_ACQUIRE, "agent");
;             xb_add(&bar[XB_XGEN(b.x)], 1u);
;             asm volatile("s_waitcnt vmcnt(0)" ::: "memory");
;         } else {
;             XB_SPIN(xb_ld(&bar[XB_XGEN(b.x)]) == gen, bar);
;             __builtin_amdgcn_fence(__ATOMIC_ACQUIRE, "agent");
;             asm volatile("s_waitcnt vmcnt(0)" ::: "memory");
;         }
;     }
;     __syncthreads();
; }
; template <int L>
; __device__ __forceinline__ void layer(Frame& F, const XcdBarrier& bar, float* out, const int lo, const int hi) {
;     ...
;         SEAM(pb + 7);
.LBB0_1321:
	v_readlane_b32 s0, v255, 11
	v_readlane_b32 s1, v255, 12
	s_cmp_gt_i32 s1, 10
	s_cselect_b64 s[0:1], -1, 0
	s_and_b64 s[6:7], s[28:29], s[0:1]
	s_andn2_b64 vcc, exec, s[6:7]
	s_cbranch_vccnz .LBB0_1375
	s_waitcnt vmcnt(0)
	s_waitcnt vmcnt(0) lgkmcnt(0)
	s_barrier
	s_mov_b64 s[6:7], exec
	v_readlane_b32 s8, v255, 7
	v_readlane_b32 s9, v255, 8
	s_and_b64 s[8:9], s[6:7], s[8:9]
	s_mov_b64 exec, s[8:9]
	s_cbranch_execz .LBB0_1374
	s_add_i32 s3, 0, 0x20160
	v_mov_b32_e32 v1, s3
	ds_read_b64 v[2:3], v1
	v_readlane_b32 s8, v255, 6
	s_lshl_b32 s9, s8, 8
	s_add_u32 s10, s9, 0x5400
	v_mov_b32_e32 v4, s10
	v_mov_b32_e32 v5, 1
	s_waitcnt lgkmcnt(0)
	v_readfirstlane_b32 s12, v2
	v_readfirstlane_b32 s13, v3
	global_atomic_add v6, v4, v5, s[50:51] sc0
	s_add_u32 s14, s101, 1
	s_mul_i32 s15, s14, s12
	s_mul_i32 s16, s14, s13
	s_add_u32 s17, s9, 0x6400
	v_mov_b32_e32 v7, s17
	s_waitcnt vmcnt(0)
	v_readfirstlane_b32 s18, v6
	s_add_u32 s18, s18, 1
	s_cmp_lg_u32 s18, s15
	s_cbranch_scc1 .Lgb10_wait
	buffer_wbl2 sc1
	s_waitcnt vmcnt(0)
	v_mov_b32_e32 v8, 0x7400
	global_atomic_add v8, v5, s[50:51]

; __device__ __forceinline__ unsigned xb_ld(unsigned* p)              { return __hip_atomic_load(p, __ATOMIC_RELAXED, __HIP_MEMORY_SCOPE_AGENT); }
; __device__ __forceinline__ unsigned xb_add(unsigned* p, unsigned v) { return __hip_atomic_fetch_add(p, v, __ATOMIC_RELAXED, __HIP_MEMORY_SCOPE_AGENT); }
; #define XB_SPIN(cond, bar) do { unsigned _sp = 0; while (cond) { __builtin_amdgcn_s_sleep(1); \
;     if ((++_sp & 255u) == 0u) { if (xb_ld(&(bar)[XB_TMO])) break; if (_sp > XB_SPIN_CAP) { atomicAdd(&(bar)[XB_TMO], 1u); break; } } } } while (0)
; #define SEAM(k) do { if (IN(k) && IN((k) + 1)) GRID_BAR(); } while (0)
; __device__ __forceinline__ void xcd_barrier(const XcdBarrier& b) {
;     asm volatile("s_waitcnt vmcnt(0)" ::: "memory");
;     __syncthreads();
;     if (threadIdx.x == 0) {
;         unsigned* bar = b.bar;
;         __builtin_amdgcn_s_waitcnt(0);
;         unsigned nloc = b.st[0], nx = b.st[1];
;         if (nloc == 0u) { xcd_barrier_complete(bar, b.x, nloc, nx); b.st[0] = nloc; b.st[1] = nx; }
;         const unsigned old = xb_add(&bar[XB_XSUB(b.x)], 1u);
;         const unsigned gen = old / nloc;
;         if (old + 1u == (gen + 1u) * nloc) {
;             __builtin_amdgcn_fence(__ATOMIC_RELEASE, "agent");
;             asm volatile("s_waitcnt vmcnt(0)" ::: "memory");
;             const unsigned og = xb_add(&bar[XB_TOP], 1u);
;             const unsigned tg = og / nx;
;             if (og + 1u == (tg + 1u) * nx) xb_add(&bar[XB_TOPGEN], 1u);
;             else XB_SPIN(xb_ld(&bar[XB_TOPGEN]) == tg, bar);
;             __builtin_amdgcn_fence(__ATOMIC_ACQUIRE, "agent");
;             xb_add(&bar[XB_XGEN(b.x)], 1u);
;             asm volatile("s_waitcnt vmcnt(0)" ::: "memory");
;         } else {
;             XB_SPIN(xb_ld(&bar[XB_XGEN(b.x)]) == gen, bar);
;             __builtin_amdgcn_fence(__ATOMIC_ACQUIRE, "agent");
;             asm volatile("s_waitcnt vmcnt(0)" ::: "memory");
;         }
;     }
;     __syncthreads();
; }
; template <int L>
; __device__ __forceinline__ void layer(Frame& F, const XcdBarrier& bar, float* out, const int lo, const int hi) {
;     ...
;     SEAM(pb + 0);
.LBB0_1407:
	v_readlane_b32 s0, v255, 11
	v_readlane_b32 s1, v255, 12
	s_cmp_gt_i32 s1, 11
	s_cselect_b64 s[6:7], -1, 0
	s_and_b64 s[0:1], s[12:13], s[6:7]
	s_andn2_b64 vcc, exec, s[0:1]
	s_cbranch_vccnz .LBB0_1461
	s_waitcnt vmcnt(0)
	s_waitcnt vmcnt(0) lgkmcnt(0)
	s_barrier
	s_mov_b64 s[0:1], exec
	v_readlane_b32 s8, v255, 7
	v_readlane_b32 s9, v255, 8
	s_and_b64 s[8:9], s[0:1], s[8:9]
	s_mov_b64 exec, s[8:9]
	s_cbranch_execz .LBB0_1460
	s_add_i32 s3, 0, 0x20160
	v_mov_b32_e32 v1, s3
	ds_read_b64 v[2:3], v1
	v_readlane_b32 s8, v255, 6
	s_lshl_b32 s9, s8, 8
	s_add_u32 s10, s9, 0x5400
	v_mov_b32_e32 v4, s10
	v_mov_b32_e32 v5, 1
	s_waitcnt lgkmcnt(0)
	v_readfirstlane_b32 s12, v2
	v_readfirstlane_b32 s13, v3
	global_atomic_add v6, v4, v5, s[50:51] sc0
	s_add_u32 s14, s101, 1
	s_mul_i32 s15, s14, s12
	s_mul_i32 s16, s14, s13
	s_add_u32 s17, s9, 0x6400
	v_mov_b32_e32 v7, s17
	s_waitcnt vmcnt(0)
	v_readfirstlane_b32 s18, v6
	s_add_u32 s18, s18, 1
	s_cmp_lg_u32 s18, s15
	s_cbranch_scc1 .Lgb11_wait
	buffer_wbl2 sc1
	s_waitcnt vmcnt(0)
	v_mov_b32_e32 v8, 0x7400
	global_atomic_add v8, v5, s[50:51]

; __device__ __forceinline__ unsigned xb_ld(unsigned* p)              { return __hip_atomic_load(p, __ATOMIC_RELAXED, __HIP_MEMORY_SCOPE_AGENT); }
; __device__ __forceinline__ unsigned xb_add(unsigned* p, unsigned v) { return __hip_atomic_fetch_add(p, v, __ATOMIC_RELAXED, __HIP_MEMORY_SCOPE_AGENT); }
; #define XB_SPIN(cond, bar) do { unsigned _sp = 0; while (cond) { __builtin_amdgcn_s_sleep(1); \
;     if ((++_sp & 255u) == 0u) { if (xb_ld(&(bar)[XB_TMO])) break; if (_sp > XB_SPIN_CAP) { atomicAdd(&(bar)[XB_TMO], 1u); break; } } } } while (0)
; #define SEAM(k) do { if (IN(k) && IN((k) + 1)) GRID_BAR(); } while (0)
; __device__ __forceinline__ void xcd_barrier(const XcdBarrier& b) {
;     asm volatile("s_waitcnt vmcnt(0)" ::: "memory");
;     __syncthreads();
;     if (threadIdx.x == 0) {
;         unsigned* bar = b.bar;
;         __builtin_amdgcn_s_waitcnt(0);
;         unsigned nloc = b.st[0], nx = b.st[1];
;         if (nloc == 0u) { xcd_barrier_complete(bar, b.x, nloc, nx); b.st[0] = nloc; b.st[1] = nx; }
;         const unsigned old = xb_add(&bar[XB_XSUB(b.x)], 1u);
;         const unsigned gen = old / nloc;
;         if (old + 1u == (gen + 1u) * nloc) {
;             __builtin_amdgcn_fence(__ATOMIC_RELEASE, "agent");
;             asm volatile("s_waitcnt vmcnt(0)" ::: "memory");
;             const unsigned og = xb_add(&bar[XB_TOP], 1u);
;             const unsigned tg = og / nx;
;             if (og + 1u == (tg + 1u) * nx) xb_add(&bar[XB_TOPGEN], 1u);
;             else XB_SPIN(xb_ld(&bar[XB_TOPGEN]) == tg, bar);
;             __builtin_amdgcn_fence(__ATOMIC_ACQUIRE, "agent");
;             xb_add(&bar[XB_XGEN(b.x)], 1u);
;             asm volatile("s_waitcnt vmcnt(0)" ::: "memory");
;         } else {
;             XB_SPIN(xb_ld(&bar[XB_XGEN(b.x)]) == gen, bar);
;             __builtin_amdgcn_fence(__ATOMIC_ACQUIRE, "agent");
;             asm volatile("s_waitcnt vmcnt(0)" ::: "memory");
;         }
;     }
;     __syncthreads();
; }
; template <int L>
; __device__ __forceinline__ void layer(Frame& F, const XcdBarrier& bar, float* out, const int lo, const int hi) {
;     ...
;     SEAM(pb + 1);
.LBB0_1486:
	v_readlane_b32 s6, v255, 11
	v_readlane_b32 s7, v255, 12
	s_cmp_gt_i32 s7, 12
	s_cselect_b64 s[6:7], -1, 0
	s_and_b64 s[0:1], s[0:1], s[6:7]
	s_andn2_b64 vcc, exec, s[0:1]
	s_cbranch_vccnz .LBB0_1540
	s_waitcnt vmcnt(0)
	s_waitcnt vmcnt(0) lgkmcnt(0)
	s_barrier
	s_mov_b64 s[0:1], exec
	v_readlane_b32 s8, v255, 7
	v_readlane_b32 s9, v255, 8
	s_and_b64 s[8:9], s[0:1], s[8:9]
	s_mov_b64 exec, s[8:9]
	s_cbranch_execz .LBB0_1539
	s_add_i32 s3, 0, 0x20160
	v_mov_b32_e32 v1, s3
	ds_read_b64 v[2:3], v1
	v_readlane_b32 s8, v255, 6
	s_lshl_b32 s9, s8, 8
	s_add_u32 s10, s9, 0x5400
	v_mov_b32_e32 v4, s10
	v_mov_b32_e32 v5, 1
	s_waitcnt lgkmcnt(0)
	v_readfirstlane_b32 s12, v2
	v_readfirstlane_b32 s13, v3
	global_atomic_add v6, v4, v5, s[50:51] sc0
	s_add_u32 s14, s101, 1
	s_mul_i32 s15, s14, s12
	s_mul_i32 s16, s14, s13
	s_add_u32 s17, s9, 0x6400
	v_mov_b32_e32 v7, s17
	s_waitcnt vmcnt(0)
	v_readfirstlane_b32 s18, v6
	s_add_u32 s18, s18, 1
	s_cmp_lg_u32 s18, s15
	s_cbranch_scc1 .Lgb12_wait
	buffer_wbl2 sc1
	s_waitcnt vmcnt(0)
	v_mov_b32_e32 v8, 0x7400
	global_atomic_add v8, v5, s[50:51]

; __device__ __forceinline__ unsigned xb_ld(unsigned* p)              { return __hip_atomic_load(p, __ATOMIC_RELAXED, __HIP_MEMORY_SCOPE_AGENT); }
; __device__ __forceinline__ unsigned xb_add(unsigned* p, unsigned v) { return __hip_atomic_fetch_add(p, v, __ATOMIC_RELAXED, __HIP_MEMORY_SCOPE_AGENT); }
; #define XB_SPIN(cond, bar) do { unsigned _sp = 0; while (cond) { __builtin_amdgcn_s_sleep(1); \
;     if ((++_sp & 255u) == 0u) { if (xb_ld(&(bar)[XB_TMO])) break; if (_sp > XB_SPIN_CAP) { atomicAdd(&(bar)[XB_TMO], 1u); break; } } } } while (0)
; #define GRID_BAR() do { if (N_LAUNCHES == 1) xcd_barrier(bar); } while (0)
; __device__ __forceinline__ void xcd_barrier(const XcdBarrier& b) {
;     asm volatile("s_waitcnt vmcnt(0)" ::: "memory");
;     __syncthreads();
;     if (threadIdx.x == 0) {
;         unsigned* bar = b.bar;
;         __builtin_amdgcn_s_waitcnt(0);
;         unsigned nloc = b.st[0], nx = b.st[1];
;         if (nloc == 0u) { xcd_barrier_complete(bar, b.x, nloc, nx); b.st[0] = nloc; b.st[1] = nx; }
;         const unsigned old = xb_add(&bar[XB_XSUB(b.x)], 1u);
;         const unsigned gen = old / nloc;
;         if (old + 1u == (gen + 1u) * nloc) {
;             __builtin_amdgcn_fence(__ATOMIC_RELEASE, "agent");
;             asm volatile("s_waitcnt vmcnt(0)" ::: "memory");
;             const unsigned og = xb_add(&bar[XB_TOP], 1u);
;             const unsigned tg = og / nx;
;             if (og + 1u == (tg + 1u) * nx) xb_add(&bar[XB_TOPGEN], 1u);
;             else XB_SPIN(xb_ld(&bar[XB_TOPGEN]) == tg, bar);
;             __builtin_amdgcn_fence(__ATOMIC_ACQUIRE, "agent");
;             xb_add(&bar[XB_XGEN(b.x)], 1u);
;             asm volatile("s_waitcnt vmcnt(0)" ::: "memory");
;         } else {
;             XB_SPIN(xb_ld(&bar[XB_XGEN(b.x)]) == gen, bar);
;             __builtin_amdgcn_fence(__ATOMIC_ACQUIRE, "agent");
;             asm volatile("s_waitcnt vmcnt(0)" ::: "memory");
;         }
;     }
;     __syncthreads();
; }
; template <int L>
; __device__ __forceinline__ void layer(Frame& F, const XcdBarrier& bar, float* out, const int lo, const int hi) {
;     ...
;         GRID_BAR();
.LBB0_1617:
	s_waitcnt vmcnt(0)
	s_waitcnt vmcnt(0) lgkmcnt(0)
	s_barrier
	s_mov_b64 s[0:1], exec
	v_readlane_b32 s6, v255, 7
	v_readlane_b32 s7, v255, 8
	s_and_b64 s[6:7], s[0:1], s[6:7]
	s_mov_b64 exec, s[6:7]
	s_cbranch_execz .LBB0_1669
	s_add_i32 s3, 0, 0x20160
	v_mov_b32_e32 v1, s3
	ds_read_b64 v[2:3], v1
	v_readlane_b32 s8, v255, 6
	s_lshl_b32 s9, s8, 8
	s_add_u32 s10, s9, 0x5400
	v_mov_b32_e32 v4, s10
	v_mov_b32_e32 v5, 1
	s_waitcnt lgkmcnt(0)
	v_readfirstlane_b32 s12, v2
	v_readfirstlane_b32 s13, v3
	global_atomic_add v6, v4, v5, s[50:51] sc0
	s_add_u32 s14, s101, 1
	s_mul_i32 s15, s14, s12
	s_mul_i32 s16, s14, s13
	s_add_u32 s17, s9, 0x6400
	v_mov_b32_e32 v7, s17
	s_waitcnt vmcnt(0)
	v_readfirstlane_b32 s18, v6
	s_add_u32 s18, s18, 1
	s_cmp_lg_u32 s18, s15
	s_cbranch_scc1 .Lgb13_wait
	buffer_wbl2 sc1
	s_waitcnt vmcnt(0)
	v_mov_b32_e32 v8, 0x7400
	global_atomic_add v8, v5, s[50:51]

; __device__ __forceinline__ unsigned xb_ld(unsigned* p)              { return __hip_atomic_load(p, __ATOMIC_RELAXED, __HIP_MEMORY_SCOPE_AGENT); }
; __device__ __forceinline__ unsigned xb_add(unsigned* p, unsigned v) { return __hip_atomic_fetch_add(p, v, __ATOMIC_RELAXED, __HIP_MEMORY_SCOPE_AGENT); }
; #define XB_SPIN(cond, bar) do { unsigned _sp = 0; while (cond) { __builtin_amdgcn_s_sleep(1); \
;     if ((++_sp & 255u) == 0u) { if (xb_ld(&(bar)[XB_TMO])) break; if (_sp > XB_SPIN_CAP) { atomicAdd(&(bar)[XB_TMO], 1u); break; } } } } while (0)
; #define SEAM(k) do { if (IN(k) && IN((k) + 1)) GRID_BAR(); } while (0)
; __device__ __forceinline__ void xcd_barrier(const XcdBarrier& b) {
;     asm volatile("s_waitcnt vmcnt(0)" ::: "memory");
;     __syncthreads();
;     if (threadIdx.x == 0) {
;         unsigned* bar = b.bar;
;         __builtin_amdgcn_s_waitcnt(0);
;         unsigned nloc = b.st[0], nx = b.st[1];
;         if (nloc == 0u) { xcd_barrier_complete(bar, b.x, nloc, nx); b.st[0] = nloc; b.st[1] = nx; }
;         const unsigned old = xb_add(&bar[XB_XSUB(b.x)], 1u);
;         const unsigned gen = old / nloc;
;         if (old + 1u == (gen + 1u) * nloc) {
;             __builtin_amdgcn_fence(__ATOMIC_RELEASE, "agent");
;             asm volatile("s_waitcnt vmcnt(0)" ::: "memory");
;             const unsigned og = xb_add(&bar[XB_TOP], 1u);
;             const unsigned tg = og / nx;
;             if (og + 1u == (tg + 1u) * nx) xb_add(&bar[XB_TOPGEN], 1u);
;             else XB_SPIN(xb_ld(&bar[XB_TOPGEN]) == tg, bar);
;             __builtin_amdgcn_fence(__ATOMIC_ACQUIRE, "agent");
;             xb_add(&bar[XB_XGEN(b.x)], 1u);
;             asm volatile("s_waitcnt vmcnt(0)" ::: "memory");
;         } else {
;             XB_SPIN(xb_ld(&bar[XB_XGEN(b.x)]) == gen, bar);
;             __builtin_amdgcn_fence(__ATOMIC_ACQUIRE, "agent");
;             asm volatile("s_waitcnt vmcnt(0)" ::: "memory");
;         }
;     }
;     __syncthreads();
; }
; template <int L>
; __device__ __forceinline__ void layer(Frame& F, const XcdBarrier& bar, float* out, const int lo, const int hi) {
;     ...
;     SEAM(pb + 2);
.LBB0_2036:
	v_readlane_b32 s0, v255, 11
	v_readlane_b32 s1, v255, 12
	s_cmp_gt_i32 s1, 13
	v_readlane_b32 s0, v255, 37
	s_cselect_b64 s[6:7], -1, 0
	v_readlane_b32 s1, v255, 38
	s_and_b64 s[0:1], s[0:1], s[6:7]
	s_andn2_b64 vcc, exec, s[0:1]
	s_cbranch_vccnz .LBB0_2090
	s_waitcnt vmcnt(0)
	s_waitcnt vmcnt(0) lgkmcnt(0)
	s_barrier
	s_mov_b64 s[0:1], exec
	v_readlane_b32 s8, v255, 7
	v_readlane_b32 s9, v255, 8
	s_and_b64 s[8:9], s[0:1], s[8:9]
	s_mov_b64 exec, s[8:9]
	s_cbranch_execz .LBB0_2089
	s_add_i32 s3, 0, 0x20160
	v_mov_b32_e32 v1, s3
	ds_read_b64 v[2:3], v1
	v_readlane_b32 s8, v255, 6
	s_lshl_b32 s9, s8, 8
	s_add_u32 s10, s9, 0x5400
	v_mov_b32_e32 v4, s10
	v_mov_b32_e32 v5, 1
	s_waitcnt lgkmcnt(0)
	v_readfirstlane_b32 s12, v2
	v_readfirstlane_b32 s13, v3
	global_atomic_add v6, v4, v5, s[50:51] sc0
	s_add_u32 s14, s101, 1
	s_mul_i32 s15, s14, s12
	s_mul_i32 s16, s14, s13
	s_add_u32 s17, s9, 0x6400
	v_mov_b32_e32 v7, s17
	s_waitcnt vmcnt(0)
	v_readfirstlane_b32 s18, v6
	s_add_u32 s18, s18, 1
	s_cmp_lg_u32 s18, s15
	s_cbranch_scc1 .Lgb14_wait
	buffer_wbl2 sc1
	s_waitcnt vmcnt(0)
	v_mov_b32_e32 v8, 0x7400
	global_atomic_add v8, v5, s[50:51]

; __device__ __forceinline__ unsigned xb_ld(unsigned* p)              { return __hip_atomic_load(p, __ATOMIC_RELAXED, __HIP_MEMORY_SCOPE_AGENT); }
; __device__ __forceinline__ unsigned xb_add(unsigned* p, unsigned v) { return __hip_atomic_fetch_add(p, v, __ATOMIC_RELAXED, __HIP_MEMORY_SCOPE_AGENT); }
; #define XB_SPIN(cond, bar) do { unsigned _sp = 0; while (cond) { __builtin_amdgcn_s_sleep(1); \
;     if ((++_sp & 255u) == 0u) { if (xb_ld(&(bar)[XB_TMO])) break; if (_sp > XB_SPIN_CAP) { atomicAdd(&(bar)[XB_TMO], 1u); break; } } } } while (0)
; __device__ __forceinline__ void xcd_barrier(const XcdBarrier& b) {
;     asm volatile("s_waitcnt vmcnt(0)" ::: "memory");
;     __syncthreads();
;     if (threadIdx.x == 0) {
;         unsigned* bar = b.bar;
;         __builtin_amdgcn_s_waitcnt(0);
;         unsigned nloc = b.st[0], nx = b.st[1];
;         if (nloc == 0u) { xcd_barrier_complete(bar, b.x, nloc, nx); b.st[0] = nloc; b.st[1] = nx; }
;         const unsigned old = xb_add(&bar[XB_XSUB(b.x)], 1u);
;         const unsigned gen = old / nloc;
;         if (old + 1u == (gen + 1u) * nloc) {
;             __builtin_amdgcn_fence(__ATOMIC_RELEASE, "agent");
;             asm volatile("s_waitcnt vmcnt(0)" ::: "memory");
;             const unsigned og = xb_add(&bar[XB_TOP], 1u);
;             const unsigned tg = og / nx;
;             if (og + 1u == (tg + 1u) * nx) xb_add(&bar[XB_TOPGEN], 1u);
;             else XB_SPIN(xb_ld(&bar[XB_TOPGEN]) == tg, bar);
;             __builtin_amdgcn_fence(__ATOMIC_ACQUIRE, "agent");
;             xb_add(&bar[XB_XGEN(b.x)], 1u);
;             asm volatile("s_waitcnt vmcnt(0)" ::: "memory");
;         } else {
;             XB_SPIN(xb_ld(&bar[XB_XGEN(b.x)]) == gen, bar);
;             __builtin_amdgcn_fence(__ATOMIC_ACQUIRE, "agent");
;             asm volatile("s_waitcnt vmcnt(0)" ::: "memory");
;         }
.LBB0_2115:
	v_readlane_b32 s4, v255, 11
	v_readlane_b32 s5, v255, 12
	s_cmp_gt_i32 s5, 14
	s_cselect_b64 s[6:7], -1, 0
	s_and_b64 s[0:1], s[0:1], s[6:7]
	s_andn2_b64 vcc, exec, s[0:1]
	s_cbranch_vccnz .LBB0_2169
	s_waitcnt vmcnt(0)
	s_waitcnt vmcnt(0) lgkmcnt(0)
	s_barrier
	s_mov_b64 s[0:1], exec
	v_readlane_b32 s4, v255, 7
	v_readlane_b32 s5, v255, 8
	s_and_b64 s[4:5], s[0:1], s[4:5]
	s_mov_b64 exec, s[4:5]
	s_cbranch_execz .LBB0_2168
	s_add_i32 s3, 0, 0x20160
	v_mov_b32_e32 v1, s3
	ds_read_b64 v[2:3], v1
	v_readlane_b32 s8, v255, 6
	s_lshl_b32 s9, s8, 8
	s_add_u32 s10, s9, 0x5400
	v_mov_b32_e32 v4, s10
	v_mov_b32_e32 v5, 1
	s_waitcnt lgkmcnt(0)
	v_readfirstlane_b32 s12, v2
	v_readfirstlane_b32 s13, v3
	global_atomic_add v6, v4, v5, s[50:51] sc0
	s_add_u32 s14, s101, 1
	s_mul_i32 s15, s14, s12
	s_mul_i32 s16, s14, s13
	s_add_u32 s17, s9, 0x6400
	v_mov_b32_e32 v7, s17
	s_waitcnt vmcnt(0)
	v_readfirstlane_b32 s18, v6
	s_add_u32 s18, s18, 1
	s_cmp_lg_u32 s18, s15
	s_cbranch_scc1 .Lgb15_wait
	buffer_wbl2 sc1
	s_waitcnt vmcnt(0)
	v_mov_b32_e32 v8, 0x7400
	global_atomic_add v8, v5, s[50:51]

; __device__ __forceinline__ unsigned xb_ld(unsigned* p)              { return __hip_atomic_load(p, __ATOMIC_RELAXED, __HIP_MEMORY_SCOPE_AGENT); }
; __device__ __forceinline__ unsigned xb_add(unsigned* p, unsigned v) { return __hip_atomic_fetch_add(p, v, __ATOMIC_RELAXED, __HIP_MEMORY_SCOPE_AGENT); }
; #define XB_SPIN(cond, bar) do { unsigned _sp = 0; while (cond) { __builtin_amdgcn_s_sleep(1); \
;     if ((++_sp & 255u) == 0u) { if (xb_ld(&(bar)[XB_TMO])) break; if (_sp > XB_SPIN_CAP) { atomicAdd(&(bar)[XB_TMO], 1u); break; } } } } while (0)
; __device__ __forceinline__ void xcd_barrier(const XcdBarrier& b) {
;     asm volatile("s_waitcnt vmcnt(0)" ::: "memory");
;     __syncthreads();
;     if (threadIdx.x == 0) {
;         unsigned* bar = b.bar;
;         __builtin_amdgcn_s_waitcnt(0);
;         unsigned nloc = b.st[0], nx = b.st[1];
;         if (nloc == 0u) { xcd_barrier_complete(bar, b.x, nloc, nx); b.st[0] = nloc; b.st[1] = nx; }
;         const unsigned old = xb_add(&bar[XB_XSUB(b.x)], 1u);
;         const unsigned gen = old / nloc;
;         if (old + 1u == (gen + 1u) * nloc) {
;             __builtin_amdgcn_fence(__ATOMIC_RELEASE, "agent");
;             asm volatile("s_waitcnt vmcnt(0)" ::: "memory");
;             const unsigned og = xb_add(&bar[XB_TOP], 1u);
;             const unsigned tg = og / nx;
;             if (og + 1u == (tg + 1u) * nx) xb_add(&bar[XB_TOPGEN], 1u);
;             else XB_SPIN(xb_ld(&bar[XB_TOPGEN]) == tg, bar);
;             __builtin_amdgcn_fence(__ATOMIC_ACQUIRE, "agent");
;             xb_add(&bar[XB_XGEN(b.x)], 1u);
;             asm volatile("s_waitcnt vmcnt(0)" ::: "memory");
;         } else {
;             XB_SPIN(xb_ld(&bar[XB_XGEN(b.x)]) == gen, bar);
;             __builtin_amdgcn_fence(__ATOMIC_ACQUIRE, "agent");
;             asm volatile("s_waitcnt vmcnt(0)" ::: "memory");
;         }
.LBB0_2198:
	v_readlane_b32 s0, v255, 11
	v_readlane_b32 s1, v255, 12
	s_cmp_gt_i32 s1, 15
	s_cselect_b64 s[6:7], -1, 0
	s_and_b64 s[0:1], s[12:13], s[6:7]
	s_andn2_b64 vcc, exec, s[0:1]
	s_cbranch_vccnz .LBB0_2252
	s_waitcnt vmcnt(0)
	s_waitcnt vmcnt(0) lgkmcnt(0)
	s_barrier
	s_mov_b64 s[0:1], exec
	v_readlane_b32 s4, v255, 7
	v_readlane_b32 s5, v255, 8
	s_and_b64 s[4:5], s[0:1], s[4:5]
	s_mov_b64 exec, s[4:5]
	s_cbranch_execz .LBB0_2251
	s_add_i32 s3, 0, 0x20160
	v_mov_b32_e32 v1, s3
	ds_read_b64 v[2:3], v1
	v_readlane_b32 s8, v255, 6
	s_lshl_b32 s9, s8, 8
	s_add_u32 s10, s9, 0x5400
	v_mov_b32_e32 v4, s10
	v_mov_b32_e32 v5, 1
	s_waitcnt lgkmcnt(0)
	v_readfirstlane_b32 s12, v2
	v_readfirstlane_b32 s13, v3
	global_atomic_add v6, v4, v5, s[50:51] sc0
	s_add_u32 s14, s101, 1
	s_mul_i32 s15, s14, s12
	s_mul_i32 s16, s14, s13
	s_add_u32 s17, s9, 0x6400
	v_mov_b32_e32 v7, s17
	s_waitcnt vmcnt(0)
	v_readfirstlane_b32 s18, v6
	s_add_u32 s18, s18, 1
	s_cmp_lg_u32 s18, s15
	s_cbranch_scc1 .Lgb16_wait
	buffer_wbl2 sc1
	s_waitcnt vmcnt(0)
	v_mov_b32_e32 v8, 0x7400
	global_atomic_add v8, v5, s[50:51]

; __device__ __forceinline__ unsigned xb_ld(unsigned* p)              { return __hip_atomic_load(p, __ATOMIC_RELAXED, __HIP_MEMORY_SCOPE_AGENT); }
; __device__ __forceinline__ unsigned xb_add(unsigned* p, unsigned v) { return __hip_atomic_fetch_add(p, v, __ATOMIC_RELAXED, __HIP_MEMORY_SCOPE_AGENT); }
; #define XB_SPIN(cond, bar) do { unsigned _sp = 0; while (cond) { __builtin_amdgcn_s_sleep(1); \
;     if ((++_sp & 255u) == 0u) { if (xb_ld(&(bar)[XB_TMO])) break; if (_sp > XB_SPIN_CAP) { atomicAdd(&(bar)[XB_TMO], 1u); break; } } } } while (0)
; __device__ __forceinline__ void xcd_barrier(const XcdBarrier& b) {
;     asm volatile("s_waitcnt vmcnt(0)" ::: "memory");
;     __syncthreads();
;     if (threadIdx.x == 0) {
;         unsigned* bar = b.bar;
;         __builtin_amdgcn_s_waitcnt(0);
;         unsigned nloc = b.st[0], nx = b.st[1];
;         if (nloc == 0u) { xcd_barrier_complete(bar, b.x, nloc, nx); b.st[0] = nloc; b.st[1] = nx; }
;         const unsigned old = xb_add(&bar[XB_XSUB(b.x)], 1u);
;         const unsigned gen = old / nloc;
;         if (old + 1u == (gen + 1u) * nloc) {
;             __builtin_amdgcn_fence(__ATOMIC_RELEASE, "agent");
;             asm volatile("s_waitcnt vmcnt(0)" ::: "memory");
;             const unsigned og = xb_add(&bar[XB_TOP], 1u);
;             const unsigned tg = og / nx;
;             if (og + 1u == (tg + 1u) * nx) xb_add(&bar[XB_TOPGEN], 1u);
;             else XB_SPIN(xb_ld(&bar[XB_TOPGEN]) == tg, bar);
;             __builtin_amdgcn_fence(__ATOMIC_ACQUIRE, "agent");
;             xb_add(&bar[XB_XGEN(b.x)], 1u);
;             asm volatile("s_waitcnt vmcnt(0)" ::: "memory");
;         } else {
;             XB_SPIN(xb_ld(&bar[XB_XGEN(b.x)]) == gen, bar);
;             __builtin_amdgcn_fence(__ATOMIC_ACQUIRE, "agent");
;             asm volatile("s_waitcnt vmcnt(0)" ::: "memory");
;         }
.LBB0_2317:
	v_readlane_b32 s4, v255, 11
	v_readlane_b32 s5, v255, 12
	s_cmp_gt_i32 s5, 16
	s_cselect_b64 s[6:7], -1, 0
	s_and_b64 s[0:1], s[0:1], s[6:7]
	s_andn2_b64 vcc, exec, s[0:1]
	s_cbranch_vccnz .LBB0_2371
	s_waitcnt vmcnt(0)
	s_waitcnt vmcnt(0) lgkmcnt(0)
	s_barrier
	s_mov_b64 s[0:1], exec
	v_readlane_b32 s4, v255, 7
	v_readlane_b32 s5, v255, 8
	s_and_b64 s[4:5], s[0:1], s[4:5]
	s_mov_b64 exec, s[4:5]
	s_cbranch_execz .LBB0_2370
	s_add_i32 s3, 0, 0x20160
	v_mov_b32_e32 v1, s3
	ds_read_b64 v[2:3], v1
	v_readlane_b32 s8, v255, 6
	s_lshl_b32 s9, s8, 8
	s_add_u32 s10, s9, 0x5400
	v_mov_b32_e32 v4, s10
	v_mov_b32_e32 v5, 1
	s_waitcnt lgkmcnt(0)
	v_readfirstlane_b32 s12, v2
	v_readfirstlane_b32 s13, v3
	global_atomic_add v6, v4, v5, s[50:51] sc0
	s_add_u32 s14, s101, 1
	s_mul_i32 s15, s14, s12
	s_mul_i32 s16, s14, s13
	s_add_u32 s17, s9, 0x6400
	v_mov_b32_e32 v7, s17
	s_waitcnt vmcnt(0)
	v_readfirstlane_b32 s18, v6
	s_add_u32 s18, s18, 1
	s_cmp_lg_u32 s18, s15
	s_cbranch_scc1 .Lgb17_wait
	buffer_wbl2 sc1
	s_waitcnt vmcnt(0)
	v_mov_b32_e32 v8, 0x7400
	global_atomic_add v8, v5, s[50:51]

; __device__ __forceinline__ unsigned xb_ld(unsigned* p)              { return __hip_atomic_load(p, __ATOMIC_RELAXED, __HIP_MEMORY_SCOPE_AGENT); }
; __device__ __forceinline__ unsigned xb_add(unsigned* p, unsigned v) { return __hip_atomic_fetch_add(p, v, __ATOMIC_RELAXED, __HIP_MEMORY_SCOPE_AGENT); }
; #define XB_SPIN(cond, bar) do { unsigned _sp = 0; while (cond) { __builtin_amdgcn_s_sleep(1); \
;     if ((++_sp & 255u) == 0u) { if (xb_ld(&(bar)[XB_TMO])) break; if (_sp > XB_SPIN_CAP) { atomicAdd(&(bar)[XB_TMO], 1u); break; } } } } while (0)
; __device__ __forceinline__ void xcd_barrier(const XcdBarrier& b) {
;     asm volatile("s_waitcnt vmcnt(0)" ::: "memory");
;     __syncthreads();
;     if (threadIdx.x == 0) {
;         unsigned* bar = b.bar;
;         __builtin_amdgcn_s_waitcnt(0);
;         unsigned nloc = b.st[0], nx = b.st[1];
;         if (nloc == 0u) { xcd_barrier_complete(bar, b.x, nloc, nx); b.st[0] = nloc; b.st[1] = nx; }
;         const unsigned old = xb_add(&bar[XB_XSUB(b.x)], 1u);
;         const unsigned gen = old / nloc;
;         if (old + 1u == (gen + 1u) * nloc) {
;             __builtin_amdgcn_fence(__ATOMIC_RELEASE, "agent");
;             asm volatile("s_waitcnt vmcnt(0)" ::: "memory");
;             const unsigned og = xb_add(&bar[XB_TOP], 1u);
;             const unsigned tg = og / nx;
;             if (og + 1u == (tg + 1u) * nx) xb_add(&bar[XB_TOPGEN], 1u);
;             else XB_SPIN(xb_ld(&bar[XB_TOPGEN]) == tg, bar);
;             __builtin_amdgcn_fence(__ATOMIC_ACQUIRE, "agent");
;             xb_add(&bar[XB_XGEN(b.x)], 1u);
;             asm volatile("s_waitcnt vmcnt(0)" ::: "memory");
;         } else {
;             XB_SPIN(xb_ld(&bar[XB_XGEN(b.x)]) == gen, bar);
;             __builtin_amdgcn_fence(__ATOMIC_ACQUIRE, "agent");
;             asm volatile("s_waitcnt vmcnt(0)" ::: "memory");
;         }
.LBB0_2394:
	v_readlane_b32 s4, v255, 11
	v_readlane_b32 s5, v255, 12
	s_cmp_gt_i32 s5, 17
	s_cselect_b64 s[6:7], -1, 0
	s_and_b64 s[0:1], s[0:1], s[6:7]
	s_andn2_b64 vcc, exec, s[0:1]
	s_cbranch_vccnz .LBB0_2448
	s_waitcnt vmcnt(0)
	s_waitcnt vmcnt(0) lgkmcnt(0)
	s_barrier
	s_mov_b64 s[0:1], exec
	v_readlane_b32 s4, v255, 7
	v_readlane_b32 s5, v255, 8
	s_and_b64 s[4:5], s[0:1], s[4:5]
	s_mov_b64 exec, s[4:5]
	s_cbranch_execz .LBB0_2447
	s_add_i32 s3, 0, 0x20160
	v_mov_b32_e32 v1, s3
	ds_read_b64 v[2:3], v1
	v_readlane_b32 s8, v255, 6
	s_lshl_b32 s9, s8, 8
	s_add_u32 s10, s9, 0x5400
	v_mov_b32_e32 v4, s10
	v_mov_b32_e32 v5, 1
	s_waitcnt lgkmcnt(0)
	v_readfirstlane_b32 s12, v2
	v_readfirstlane_b32 s13, v3
	global_atomic_add v6, v4, v5, s[50:51] sc0
	s_add_u32 s14, s101, 1
	s_mul_i32 s15, s14, s12
	s_mul_i32 s16, s14, s13
	s_add_u32 s17, s9, 0x6400
	v_mov_b32_e32 v7, s17
	s_waitcnt vmcnt(0)
	v_readfirstlane_b32 s18, v6
	s_add_u32 s18, s18, 1
	s_cmp_lg_u32 s18, s15
	s_cbranch_scc1 .Lgb18_wait
	buffer_wbl2 sc1
	s_waitcnt vmcnt(0)
	v_mov_b32_e32 v8, 0x7400
	global_atomic_add v8, v5, s[50:51]
